# proj GEMM main K loops (both layers): LDS-DMA loads in SGPR-base + 32-bit lane-offset form, 16 v_lshl_add_u64 per iteration removed (scalar adds for the +0x80 K step)
# baseline (speedup 1.0000x reference)
.LBB0_271:
	ds_read_b128 v[158:161], v153
	ds_read_b128 v[162:165], v153 offset:1024
	ds_read_b128 v[166:169], v153 offset:2048
	ds_read_b128 v[170:173], v153 offset:3072
	ds_read_b128 v[174:177], v154
	ds_read_b128 v[178:181], v154 offset:1024
	ds_read_b128 v[182:185], v154 offset:2048
	ds_read_b128 v[186:189], v154 offset:3072
	s_add_u32 s30, s28, 0xfffc0080
	s_addc_u32 s31, s29, -1
	s_cmp_eq_u32 s65, 12
	s_cselect_b32 s35, s23, s31
	s_cselect_b32 s34, s22, s30
	s_cselect_b32 s31, s25, s64
	s_cselect_b32 s30, s24, s63
	s_mov_b32 m0, s19
	ds_read_b128 v[190:193], v155
	ds_read_b128 v[194:197], v155 offset:1024
	ds_read_b128 v[198:201], v155 offset:2048
	ds_read_b128 v[202:205], v155 offset:3072
	ds_read_b128 v[206:209], v155 offset:4096
	ds_read_b128 v[210:213], v155 offset:5120
	ds_read_b128 v[214:217], v155 offset:6144
	ds_read_b128 v[218:221], v155 offset:7168
	global_load_lds_dwordx4 v144, s[28:29]
	s_mov_b32 m0, s21
	s_nop 0
	global_load_lds_dwordx4 v142, s[28:29]
	s_waitcnt vmcnt(8)
	s_waitcnt lgkmcnt(0)
	s_barrier
	s_setprio 1
	s_waitcnt lgkmcnt(0)
	v_mfma_f32_16x16x32_bf16 v[116:119], v[158:161], v[190:193], v[116:119]
	v_mfma_f32_16x16x32_bf16 v[112:115], v[166:169], v[190:193], v[112:115]
	v_mfma_f32_16x16x32_bf16 v[100:103], v[158:161], v[198:201], v[100:103]
	v_mfma_f32_16x16x32_bf16 v[96:99], v[166:169], v[198:201], v[96:99]
	v_mfma_f32_16x16x32_bf16 v[84:87], v[158:161], v[206:209], v[84:87]
	v_mfma_f32_16x16x32_bf16 v[80:83], v[166:169], v[206:209], v[80:83]
	v_mfma_f32_16x16x32_bf16 v[68:71], v[158:161], v[214:217], v[68:71]
	v_mfma_f32_16x16x32_bf16 v[64:67], v[166:169], v[214:217], v[64:67]
	v_mfma_f32_16x16x32_bf16 v[116:119], v[162:165], v[194:197], v[116:119]
	v_mfma_f32_16x16x32_bf16 v[112:115], v[170:173], v[194:197], v[112:115]
	v_mfma_f32_16x16x32_bf16 v[100:103], v[162:165], v[202:205], v[100:103]
	v_mfma_f32_16x16x32_bf16 v[96:99], v[170:173], v[202:205], v[96:99]
	v_mfma_f32_16x16x32_bf16 v[84:87], v[162:165], v[210:213], v[84:87]
	v_mfma_f32_16x16x32_bf16 v[80:83], v[170:173], v[210:213], v[80:83]
	v_mfma_f32_16x16x32_bf16 v[68:71], v[162:165], v[218:221], v[68:71]
	v_mfma_f32_16x16x32_bf16 v[64:67], v[170:173], v[218:221], v[64:67]
	s_setprio 0
	s_setprio 1
	v_mfma_f32_16x16x32_bf16 v[124:127], v[174:177], v[190:193], v[124:127]
	v_mfma_f32_16x16x32_bf16 v[120:123], v[182:185], v[190:193], v[120:123]
	v_mfma_f32_16x16x32_bf16 v[108:111], v[174:177], v[198:201], v[108:111]
	v_mfma_f32_16x16x32_bf16 v[104:107], v[182:185], v[198:201], v[104:107]
	v_mfma_f32_16x16x32_bf16 v[92:95], v[174:177], v[206:209], v[92:95]
	v_mfma_f32_16x16x32_bf16 v[88:91], v[182:185], v[206:209], v[88:91]
	v_mfma_f32_16x16x32_bf16 v[76:79], v[174:177], v[214:217], v[76:79]
	v_mfma_f32_16x16x32_bf16 v[72:75], v[182:185], v[214:217], v[72:75]
	v_mfma_f32_16x16x32_bf16 v[124:127], v[178:181], v[194:197], v[124:127]
	v_mfma_f32_16x16x32_bf16 v[120:123], v[186:189], v[194:197], v[120:123]
	v_mfma_f32_16x16x32_bf16 v[108:111], v[178:181], v[202:205], v[108:111]
	v_mfma_f32_16x16x32_bf16 v[104:107], v[186:189], v[202:205], v[104:107]
	v_mfma_f32_16x16x32_bf16 v[92:95], v[178:181], v[210:213], v[92:95]
	v_mfma_f32_16x16x32_bf16 v[88:91], v[186:189], v[210:213], v[88:91]
	v_mfma_f32_16x16x32_bf16 v[76:79], v[178:181], v[218:221], v[76:79]
	v_mfma_f32_16x16x32_bf16 v[72:75], v[186:189], v[218:221], v[72:75]
	s_setprio 0
	s_barrier
	s_mov_b32 m0, s55
	s_add_u32 s66, s30, 0x40000
	ds_read_b128 v[190:193], v155 offset:16384
	ds_read_b128 v[194:197], v155 offset:17408
	ds_read_b128 v[198:201], v155 offset:18432
	ds_read_b128 v[202:205], v155 offset:19456
	ds_read_b128 v[206:209], v155 offset:20480
	ds_read_b128 v[210:213], v155 offset:21504
	ds_read_b128 v[214:217], v155 offset:22528
	ds_read_b128 v[218:221], v155 offset:23552
	global_load_lds_dwordx4 v132, s[30:31]
	s_mov_b32 m0, s56
	s_addc_u32 s67, s31, 0
	global_load_lds_dwordx4 v128, s[30:31]
	s_mov_b32 m0, s57
	s_nop 0
	global_load_lds_dwordx4 v132, s[66:67]
	s_mov_b32 m0, s58
	s_nop 0
	global_load_lds_dwordx4 v128, s[66:67]
	s_mov_b32 m0, s43
	s_nop 0
	global_load_lds_dwordx4 v134, s[34:35]
	s_mov_b32 m0, s44
	s_nop 0
	global_load_lds_dwordx4 v130, s[34:35]
	s_waitcnt vmcnt(8)
	s_waitcnt lgkmcnt(0)
	s_barrier
	s_setprio 1
	s_waitcnt lgkmcnt(0)
	v_mfma_f32_16x16x32_bf16 v[52:55], v[158:161], v[190:193], v[52:55]
	v_mfma_f32_16x16x32_bf16 v[48:51], v[166:169], v[190:193], v[48:51]
	v_mfma_f32_16x16x32_bf16 v[36:39], v[158:161], v[198:201], v[36:39]
	v_mfma_f32_16x16x32_bf16 v[32:35], v[166:169], v[198:201], v[32:35]
	v_mfma_f32_16x16x32_bf16 v[20:23], v[158:161], v[206:209], v[20:23]
	v_mfma_f32_16x16x32_bf16 v[16:19], v[166:169], v[206:209], v[16:19]
	v_mfma_f32_16x16x32_bf16 v[4:7], v[158:161], v[214:217], v[4:7]
	v_mfma_f32_16x16x32_bf16 v[0:3], v[166:169], v[214:217], v[0:3]
	v_mfma_f32_16x16x32_bf16 v[52:55], v[162:165], v[194:197], v[52:55]
	v_mfma_f32_16x16x32_bf16 v[48:51], v[170:173], v[194:197], v[48:51]
	v_mfma_f32_16x16x32_bf16 v[36:39], v[162:165], v[202:205], v[36:39]
	v_mfma_f32_16x16x32_bf16 v[32:35], v[170:173], v[202:205], v[32:35]
	v_mfma_f32_16x16x32_bf16 v[20:23], v[162:165], v[210:213], v[20:23]
	v_mfma_f32_16x16x32_bf16 v[16:19], v[170:173], v[210:213], v[16:19]
	v_mfma_f32_16x16x32_bf16 v[4:7], v[162:165], v[218:221], v[4:7]
	v_mfma_f32_16x16x32_bf16 v[0:3], v[170:173], v[218:221], v[0:3]
	s_setprio 0
	s_setprio 1
	v_mfma_f32_16x16x32_bf16 v[60:63], v[174:177], v[190:193], v[60:63]
	v_mfma_f32_16x16x32_bf16 v[56:59], v[182:185], v[190:193], v[56:59]
	v_mfma_f32_16x16x32_bf16 v[44:47], v[174:177], v[198:201], v[44:47]
	v_mfma_f32_16x16x32_bf16 v[40:43], v[182:185], v[198:201], v[40:43]
	v_mfma_f32_16x16x32_bf16 v[28:31], v[174:177], v[206:209], v[28:31]
	v_mfma_f32_16x16x32_bf16 v[24:27], v[182:185], v[206:209], v[24:27]
	v_mfma_f32_16x16x32_bf16 v[12:15], v[174:177], v[214:217], v[12:15]
	v_mfma_f32_16x16x32_bf16 v[8:11], v[182:185], v[214:217], v[8:11]
	v_mfma_f32_16x16x32_bf16 v[60:63], v[178:181], v[194:197], v[60:63]
	v_mfma_f32_16x16x32_bf16 v[56:59], v[186:189], v[194:197], v[56:59]
	v_mfma_f32_16x16x32_bf16 v[44:47], v[178:181], v[202:205], v[44:47]
	v_mfma_f32_16x16x32_bf16 v[40:43], v[186:189], v[202:205], v[40:43]
	v_mfma_f32_16x16x32_bf16 v[28:31], v[178:181], v[210:213], v[28:31]
	v_mfma_f32_16x16x32_bf16 v[24:27], v[186:189], v[210:213], v[24:27]
	v_mfma_f32_16x16x32_bf16 v[12:15], v[178:181], v[218:221], v[12:15]
	v_mfma_f32_16x16x32_bf16 v[8:11], v[186:189], v[218:221], v[8:11]
	s_setprio 0
	s_barrier
	ds_read_b128 v[158:161], v136
	ds_read_b128 v[162:165], v136 offset:1024
	ds_read_b128 v[166:169], v136 offset:2048
	ds_read_b128 v[170:173], v136 offset:3072
	ds_read_b128 v[174:177], v157
	ds_read_b128 v[178:181], v157 offset:1024
	ds_read_b128 v[182:185], v157 offset:2048
	ds_read_b128 v[186:189], v157 offset:3072
	s_add_u32 s98, s34, 0x80
	s_addc_u32 s99, s35, 0
	s_add_u32 s34, s34, 0x40000
	s_addc_u32 s35, s35, 0
	s_mov_b32 m0, s45
	ds_read_b128 v[190:193], v155 offset:32768
	ds_read_b128 v[194:197], v155 offset:33792
	ds_read_b128 v[198:201], v155 offset:34816
	ds_read_b128 v[202:205], v155 offset:35840
	ds_read_b128 v[206:209], v155 offset:36864
	ds_read_b128 v[210:213], v155 offset:37888
	ds_read_b128 v[214:217], v155 offset:38912
	ds_read_b128 v[218:221], v155 offset:39936
	global_load_lds_dwordx4 v134, s[34:35]
	s_mov_b32 m0, s46
	s_nop 0
	global_load_lds_dwordx4 v130, s[34:35]
	s_waitcnt vmcnt(8)
	s_waitcnt lgkmcnt(0)
	s_barrier
	s_setprio 1
	s_waitcnt lgkmcnt(0)
	v_mfma_f32_16x16x32_bf16 v[116:119], v[158:161], v[190:193], v[116:119]
	v_mfma_f32_16x16x32_bf16 v[112:115], v[166:169], v[190:193], v[112:115]
	v_mfma_f32_16x16x32_bf16 v[100:103], v[158:161], v[198:201], v[100:103]
	v_mfma_f32_16x16x32_bf16 v[96:99], v[166:169], v[198:201], v[96:99]
	v_mfma_f32_16x16x32_bf16 v[84:87], v[158:161], v[206:209], v[84:87]
	v_mfma_f32_16x16x32_bf16 v[80:83], v[166:169], v[206:209], v[80:83]
	v_mfma_f32_16x16x32_bf16 v[68:71], v[158:161], v[214:217], v[68:71]
	v_mfma_f32_16x16x32_bf16 v[64:67], v[166:169], v[214:217], v[64:67]
	v_mfma_f32_16x16x32_bf16 v[116:119], v[162:165], v[194:197], v[116:119]
	v_mfma_f32_16x16x32_bf16 v[112:115], v[170:173], v[194:197], v[112:115]
	v_mfma_f32_16x16x32_bf16 v[100:103], v[162:165], v[202:205], v[100:103]
	v_mfma_f32_16x16x32_bf16 v[96:99], v[170:173], v[202:205], v[96:99]
	v_mfma_f32_16x16x32_bf16 v[84:87], v[162:165], v[210:213], v[84:87]
	v_mfma_f32_16x16x32_bf16 v[80:83], v[170:173], v[210:213], v[80:83]
	v_mfma_f32_16x16x32_bf16 v[68:71], v[162:165], v[218:221], v[68:71]
	v_mfma_f32_16x16x32_bf16 v[64:67], v[170:173], v[218:221], v[64:67]
	s_setprio 0
	s_setprio 1
	v_mfma_f32_16x16x32_bf16 v[124:127], v[174:177], v[190:193], v[124:127]
	v_mfma_f32_16x16x32_bf16 v[120:123], v[182:185], v[190:193], v[120:123]
	v_mfma_f32_16x16x32_bf16 v[108:111], v[174:177], v[198:201], v[108:111]
	v_mfma_f32_16x16x32_bf16 v[104:107], v[182:185], v[198:201], v[104:107]
	v_mfma_f32_16x16x32_bf16 v[92:95], v[174:177], v[206:209], v[92:95]
	v_mfma_f32_16x16x32_bf16 v[88:91], v[182:185], v[206:209], v[88:91]
	v_mfma_f32_16x16x32_bf16 v[76:79], v[174:177], v[214:217], v[76:79]
	v_mfma_f32_16x16x32_bf16 v[72:75], v[182:185], v[214:217], v[72:75]
	v_mfma_f32_16x16x32_bf16 v[124:127], v[178:181], v[194:197], v[124:127]
	v_mfma_f32_16x16x32_bf16 v[120:123], v[186:189], v[194:197], v[120:123]
	v_mfma_f32_16x16x32_bf16 v[108:111], v[178:181], v[202:205], v[108:111]
	v_mfma_f32_16x16x32_bf16 v[104:107], v[186:189], v[202:205], v[104:107]
	v_mfma_f32_16x16x32_bf16 v[92:95], v[178:181], v[210:213], v[92:95]
	v_mfma_f32_16x16x32_bf16 v[88:91], v[186:189], v[210:213], v[88:91]
	v_mfma_f32_16x16x32_bf16 v[76:79], v[178:181], v[218:221], v[76:79]
	v_mfma_f32_16x16x32_bf16 v[72:75], v[186:189], v[218:221], v[72:75]
	s_setprio 0
	s_barrier
	s_mov_b32 m0, s59
	s_add_u32 s100, s30, 0x80
	s_addc_u32 s101, s31, 0
	ds_read_b128 v[190:193], v155 offset:49152
	ds_read_b128 v[194:197], v155 offset:50176
	ds_read_b128 v[198:201], v155 offset:51200
	ds_read_b128 v[202:205], v155 offset:52224
	ds_read_b128 v[206:209], v155 offset:53248
	ds_read_b128 v[210:213], v155 offset:54272
	ds_read_b128 v[214:217], v155 offset:55296
	ds_read_b128 v[218:221], v155 offset:56320
	global_load_lds_dwordx4 v132, s[100:101]
	s_mov_b32 m0, s60
	s_nop 0
	global_load_lds_dwordx4 v128, s[100:101]
	s_add_u32 s30, s30, 0x40080
	s_addc_u32 s31, s31, 0
	s_mov_b32 m0, s61
	s_nop 0
	global_load_lds_dwordx4 v132, s[30:31]
	s_mov_b32 m0, s62
	s_nop 0
	global_load_lds_dwordx4 v128, s[30:31]
	s_mov_b32 m0, s48
	s_nop 0
	global_load_lds_dwordx4 v134, s[98:99]
	s_mov_b32 m0, s49
	s_nop 0
	global_load_lds_dwordx4 v130, s[98:99]
	s_waitcnt vmcnt(8)
	s_waitcnt lgkmcnt(0)
	s_barrier
	s_setprio 1
	s_waitcnt lgkmcnt(0)
	v_mfma_f32_16x16x32_bf16 v[52:55], v[158:161], v[190:193], v[52:55]
	v_mfma_f32_16x16x32_bf16 v[48:51], v[166:169], v[190:193], v[48:51]
	v_mfma_f32_16x16x32_bf16 v[36:39], v[158:161], v[198:201], v[36:39]
	v_mfma_f32_16x16x32_bf16 v[32:35], v[166:169], v[198:201], v[32:35]
	v_mfma_f32_16x16x32_bf16 v[20:23], v[158:161], v[206:209], v[20:23]
	v_mfma_f32_16x16x32_bf16 v[16:19], v[166:169], v[206:209], v[16:19]
	v_mfma_f32_16x16x32_bf16 v[4:7], v[158:161], v[214:217], v[4:7]
	v_mfma_f32_16x16x32_bf16 v[0:3], v[166:169], v[214:217], v[0:3]
	v_mfma_f32_16x16x32_bf16 v[52:55], v[162:165], v[194:197], v[52:55]
	v_mfma_f32_16x16x32_bf16 v[48:51], v[170:173], v[194:197], v[48:51]
	v_mfma_f32_16x16x32_bf16 v[36:39], v[162:165], v[202:205], v[36:39]
	v_mfma_f32_16x16x32_bf16 v[32:35], v[170:173], v[202:205], v[32:35]
	v_mfma_f32_16x16x32_bf16 v[20:23], v[162:165], v[210:213], v[20:23]
	v_mfma_f32_16x16x32_bf16 v[16:19], v[170:173], v[210:213], v[16:19]
	v_mfma_f32_16x16x32_bf16 v[4:7], v[162:165], v[218:221], v[4:7]
	v_mfma_f32_16x16x32_bf16 v[0:3], v[170:173], v[218:221], v[0:3]
	s_setprio 0
	s_setprio 1
	v_mfma_f32_16x16x32_bf16 v[60:63], v[174:177], v[190:193], v[60:63]
	v_mfma_f32_16x16x32_bf16 v[56:59], v[182:185], v[190:193], v[56:59]
	v_mfma_f32_16x16x32_bf16 v[44:47], v[174:177], v[198:201], v[44:47]
	v_mfma_f32_16x16x32_bf16 v[40:43], v[182:185], v[198:201], v[40:43]
	v_mfma_f32_16x16x32_bf16 v[28:31], v[174:177], v[206:209], v[28:31]
	v_mfma_f32_16x16x32_bf16 v[24:27], v[182:185], v[206:209], v[24:27]
	v_mfma_f32_16x16x32_bf16 v[12:15], v[174:177], v[214:217], v[12:15]
	v_mfma_f32_16x16x32_bf16 v[8:11], v[182:185], v[214:217], v[8:11]
	v_mfma_f32_16x16x32_bf16 v[60:63], v[178:181], v[194:197], v[60:63]
	v_mfma_f32_16x16x32_bf16 v[56:59], v[186:189], v[194:197], v[56:59]
	v_mfma_f32_16x16x32_bf16 v[44:47], v[178:181], v[202:205], v[44:47]
	v_mfma_f32_16x16x32_bf16 v[40:43], v[186:189], v[202:205], v[40:43]
	v_mfma_f32_16x16x32_bf16 v[28:31], v[178:181], v[210:213], v[28:31]
	v_mfma_f32_16x16x32_bf16 v[24:27], v[186:189], v[210:213], v[24:27]
	v_mfma_f32_16x16x32_bf16 v[12:15], v[178:181], v[218:221], v[12:15]
	v_mfma_f32_16x16x32_bf16 v[8:11], v[186:189], v[218:221], v[8:11]
	s_setprio 0
	s_barrier
	s_add_i32 s65, s65, 2
	s_add_u32 s63, s63, 0x100
	s_addc_u32 s64, s64, 0
	s_add_u32 s28, s28, 0x100
	s_addc_u32 s29, s29, 0
	s_cmp_gt_u32 s65, 13
	s_cbranch_scc0 .LBB0_271
	s_and_b64 vcc, exec, s[12:13]
	s_cbranch_vccz .LBB0_274
	s_barrier
